# attn kernel weight-conversion tail: sc1 on the full-line dword stores of W1T/W2T (on v40)
# speedup vs baseline: 1.0066x; 1.0066x over previous
.LBB2_39:
	v_lshrrev_b32_e32 v3, 5, v0
	v_mul_u32_u24_e32 v2, 0x208, v1
	v_lshlrev_b32_e32 v6, 2, v1
	v_lshlrev_b32_e32 v1, 2, v3
	v_add3_u32 v1, 0, v2, v1
	ds_read2_b32 v[8:9], v1 offset1:8
	ds_read2_b32 v[10:11], v1 offset0:65 offset1:73
	s_ashr_i32 s19, s18, 31
	s_lshl_b64 s[0:1], s[18:19], 1
	s_add_u32 s0, s12, s0
	v_mov_b32_e32 v2, 0
	s_waitcnt lgkmcnt(1)
	v_mov_b32_e32 v12, v8
	s_waitcnt lgkmcnt(0)
	v_mov_b32_e32 v13, v10
	s_addc_u32 s1, s13, s1
	v_mov_b32_e32 v7, v2
	v_pk_mul_f32 v[12:13], v[4:5], v[12:13]
	v_or_b32_e32 v14, s16, v3
	v_lshl_add_u64 v[6:7], s[0:1], 0, v[6:7]
	v_cvt_pk_f16_f32 v8, v12, v13
	v_mad_i64_i32 v[12:13], s[0:1], v14, s22, 0
	v_lshl_add_u64 v[12:13], v[12:13], 1, v[6:7]
	v_mov_b32_e32 v10, v9
	global_store_dword v[12:13], v8, off sc1
	v_pk_mul_f32 v[8:9], v[4:5], v[10:11]
	v_add_u32_e32 v3, s16, v3
	v_cvt_pk_f16_f32 v15, v8, v9
	ds_read2_b32 v[8:9], v1 offset0:16 offset1:24
	ds_read2_b32 v[10:11], v1 offset0:81 offset1:89
	v_add_u32_e32 v12, 8, v3
	v_mad_i64_i32 v[12:13], s[0:1], v12, s22, 0
	v_lshl_add_u64 v[12:13], v[12:13], 1, v[6:7]
	global_store_dword v[12:13], v15, off sc1
	s_waitcnt lgkmcnt(1)
	v_mov_b32_e32 v12, v8
	s_waitcnt lgkmcnt(0)
	v_mov_b32_e32 v13, v10
	v_pk_mul_f32 v[12:13], v[4:5], v[12:13]
	v_add_u32_e32 v10, 16, v3
	v_cvt_pk_f16_f32 v8, v12, v13
	v_mad_i64_i32 v[12:13], s[0:1], v10, s22, 0
	v_lshl_add_u64 v[12:13], v[12:13], 1, v[6:7]
	v_mov_b32_e32 v10, v9
	global_store_dword v[12:13], v8, off sc1
	v_pk_mul_f32 v[8:9], v[4:5], v[10:11]
	v_add_u32_e32 v12, 24, v3
	v_cvt_pk_f16_f32 v15, v8, v9
	ds_read2_b32 v[8:9], v1 offset0:32 offset1:40
	ds_read2_b32 v[10:11], v1 offset0:97 offset1:105
	v_mad_i64_i32 v[12:13], s[0:1], v12, s22, 0
	v_lshl_add_u64 v[12:13], v[12:13], 1, v[6:7]
	global_store_dword v[12:13], v15, off sc1
	s_waitcnt lgkmcnt(1)
	v_mov_b32_e32 v12, v8
	s_waitcnt lgkmcnt(0)
	v_mov_b32_e32 v13, v10
	v_pk_mul_f32 v[12:13], v[4:5], v[12:13]
	v_or_b32_e32 v10, 32, v14
	v_cvt_pk_f16_f32 v8, v12, v13
	v_mad_i64_i32 v[12:13], s[0:1], v10, s22, 0
	v_lshl_add_u64 v[12:13], v[12:13], 1, v[6:7]
	v_mov_b32_e32 v10, v9
	global_store_dword v[12:13], v8, off sc1
	v_pk_mul_f32 v[8:9], v[4:5], v[10:11]
	v_add_u32_e32 v12, 40, v3
	v_cvt_pk_f16_f32 v14, v8, v9
	ds_read2_b32 v[8:9], v1 offset0:48 offset1:56
	ds_read2_b32 v[10:11], v1 offset0:113 offset1:121
	v_mad_i64_i32 v[12:13], s[0:1], v12, s22, 0
	v_lshl_add_u64 v[12:13], v[12:13], 1, v[6:7]
	global_store_dword v[12:13], v14, off sc1
	s_waitcnt lgkmcnt(1)
	v_mov_b32_e32 v12, v8
	s_waitcnt lgkmcnt(0)
	v_mov_b32_e32 v13, v10
	v_pk_mul_f32 v[12:13], v[4:5], v[12:13]
	v_add_u32_e32 v8, 48, v3
	v_cvt_pk_f16_f32 v1, v12, v13
	v_mad_i64_i32 v[12:13], s[0:1], v8, s22, 0
	v_mov_b32_e32 v10, v9
	v_lshl_add_u64 v[12:13], v[12:13], 1, v[6:7]
	v_pk_mul_f32 v[4:5], v[4:5], v[10:11]
	v_add_u32_e32 v3, 56, v3
	global_store_dword v[12:13], v1, off sc1
	v_cvt_pk_f16_f32 v1, v4, v5
	v_mad_i64_i32 v[4:5], s[0:1], v3, s22, 0
	v_lshl_add_u64 v[4:5], v[4:5], 1, v[6:7]
	global_store_dword v[4:5], v1, off sc1
	s_and_saveexec_b64 s[0:1], s[14:15]
	s_cbranch_execz .LBB2_43
	v_lshlrev_b32_e32 v1, 2, v0
	s_movk_i32 s0, 0x4100
	v_mov_b32_e32 v3, v2
